# baseline (speedup 1.0000x reference)
.LBB1_71:
	s_mov_b32 s49, 0x12345678
	s_mov_b32 s49, 0x12345678
	s_mov_b32 s49, 0x12345678
	s_mov_b32 s49, 0x12345678
	s_mov_b32 s49, 0x12345678
	s_mov_b32 s49, 0x12345678
	s_mov_b32 s49, 0x12345678
	s_mov_b32 s49, 0x12345678
	s_mov_b32 s49, 0x12345678
	s_mov_b32 s49, 0x12345678
	s_mov_b32 s49, 0x12345678
	s_mov_b32 s49, 0x12345678
	s_mov_b32 s49, 0x12345678
	s_mov_b32 s49, 0x12345678
	s_mov_b32 s49, 0x12345678
	s_mov_b32 s49, 0x12345678
	s_mov_b32 s49, 0x12345678
	s_mov_b32 s49, 0x12345678
	s_mov_b32 s49, 0x12345678
	s_mov_b32 s49, 0x12345678
	s_mov_b32 s49, 0x12345678
	s_mov_b32 s49, 0x12345678
	s_mov_b32 s49, 0x12345678
	s_mov_b32 s49, 0x12345678
	s_mov_b32 s49, 0x12345678
	s_mov_b32 s49, 0x12345678
	s_mov_b32 s49, 0x12345678
	s_mov_b32 s49, 0x12345678
	s_mov_b32 s49, 0x12345678
	s_mov_b32 s49, 0x12345678
	s_mov_b32 s49, 0x12345678
	s_mov_b32 s49, 0x12345678
	s_mov_b32 s49, 0x12345678
	s_mov_b32 s49, 0x12345678
	s_mov_b32 s49, 0x12345678
	s_mov_b32 s49, 0x12345678
	s_mov_b32 s49, 0x12345678
	s_mov_b32 s49, 0x12345678
	s_mov_b32 s49, 0x12345678
	s_mov_b32 s49, 0x12345678
	s_mov_b32 s49, 0x12345678
	s_mov_b32 s49, 0x12345678
	s_mov_b32 s49, 0x12345678
	s_mov_b32 s49, 0x12345678
	s_mov_b32 s49, 0x12345678
	s_mov_b32 s49, 0x12345678
	s_mov_b32 s49, 0x12345678
	s_mov_b32 s49, 0x12345678
	s_mov_b32 s49, 0x12345678
	s_mov_b32 s49, 0x12345678
	s_mov_b32 s49, 0x12345678
	s_mov_b32 s49, 0x12345678
	s_mov_b32 s49, 0x12345678
	s_mov_b32 s49, 0x12345678
	s_mov_b32 s49, 0x12345678
	s_mov_b32 s49, 0x12345678
	s_mov_b32 s49, 0x12345678
	s_mov_b32 s49, 0x12345678
	s_mov_b32 s49, 0x12345678
	s_mov_b32 s49, 0x12345678
	s_mov_b32 s49, 0x12345678
	s_mov_b32 s49, 0x12345678
	s_mov_b32 s49, 0x12345678
	s_mov_b32 s49, 0x12345678
	s_mov_b32 s49, 0x12345678
	s_mov_b32 s49, 0x12345678
	s_mov_b32 s49, 0x12345678
	s_mov_b32 s49, 0x12345678
	s_mov_b32 s49, 0x12345678
	s_mov_b32 s49, 0x12345678
	s_mov_b32 s49, 0x12345678
	s_mov_b32 s49, 0x12345678
	s_mov_b32 s49, 0x12345678
	s_mov_b32 s49, 0x12345678
	s_mov_b32 s49, 0x12345678
	s_mov_b32 s49, 0x12345678
	s_mov_b32 s49, 0x12345678
	s_mov_b32 s49, 0x12345678
	s_mov_b32 s49, 0x12345678
	s_mov_b32 s49, 0x12345678
	s_mov_b32 s49, 0x12345678
	s_mov_b32 s49, 0x12345678
	s_mov_b32 s49, 0x12345678
	s_mov_b32 s49, 0x12345678
	s_mov_b32 s49, 0x12345678
	s_mov_b32 s49, 0x12345678
	s_mov_b32 s49, 0x12345678
	s_mov_b32 s49, 0x12345678
	s_mov_b32 s49, 0x12345678
	s_mov_b32 s49, 0x12345678
	s_mov_b32 s49, 0x12345678
	s_mov_b32 s49, 0x12345678
	s_mov_b32 s49, 0x12345678
	s_mov_b32 s49, 0x12345678
	s_mov_b32 s49, 0x12345678
	s_mov_b32 s49, 0x12345678
	s_mov_b32 s49, 0x12345678
	s_mov_b32 s49, 0x12345678
	s_mov_b32 s49, 0x12345678
	s_mov_b32 s49, 0x12345678
	s_mov_b32 s49, 0x12345678
	s_mov_b32 s49, 0x12345678
	s_mov_b32 s49, 0x12345678
	s_mov_b32 s49, 0x12345678
	s_mov_b32 s49, 0x12345678
	s_mov_b32 s49, 0x12345678
	s_mov_b32 s49, 0x12345678
	s_mov_b32 s49, 0x12345678
	s_mov_b32 s49, 0x12345678
	s_mov_b32 s49, 0x12345678
	s_mov_b32 s49, 0x12345678
	s_mov_b32 s49, 0x12345678
	s_mov_b32 s49, 0x12345678
	s_mov_b32 s49, 0x12345678
	s_mov_b32 s49, 0x12345678
	s_mov_b32 s49, 0x12345678
	s_mov_b32 s49, 0x12345678
	s_mov_b32 s49, 0x12345678
	s_mov_b32 s49, 0x12345678
	s_mov_b32 s49, 0x12345678
	s_mov_b32 s49, 0x12345678
	s_mov_b32 s49, 0x12345678
	s_mov_b32 s49, 0x12345678
	s_mov_b32 s49, 0x12345678
	s_mov_b32 s49, 0x12345678
	s_mov_b32 s49, 0x12345678
	s_mov_b32 s49, 0x12345678
	s_mov_b32 s49, 0x12345678
	s_mul_i32 s1, s33, 0xe10
	s_mul_hi_u32 s0, s33, 0xe10
	s_add_u32 s38, s36, s1
	s_addc_u32 s39, s37, s0
	s_mul_hi_u32 s0, s33, 0x4b0
	s_mulk_i32 s33, 0x4b0
	s_add_u32 s1, s36, s33
	s_addc_u32 s0, s37, s0
	s_add_u32 s36, s1, 0x274200
	s_addc_u32 s37, s0, 0
	s_andn2_b64 vcc, exec, s[2:3]
	s_mov_b64 s[0:1], -1
	s_cbranch_vccnz .LBB1_94
	v_sub_u32_e32 v4, v26, v17
	s_waitcnt lgkmcnt(0)
	v_add_u32_e32 v5, v35, v4
	v_add_u32_e32 v4, v5, v7
	s_movk_i32 s0, 0x12c
	ds_write_b64 v9, v[4:5]
	v_cmp_gt_i32_e32 vcc, s0, v5
	v_add_u32_e32 v5, v4, v6
	s_movk_i32 s2, 0x12b
	v_cmp_lt_i32_e64 s[0:1], s2, v5
	s_and_b64 s[8:9], vcc, s[0:1]
	s_and_saveexec_b64 s[0:1], s[8:9]
	s_cbranch_execz .LBB1_74
	v_cmp_lt_i32_e32 vcc, s2, v4
	v_mov_b32_e32 v6, 0
	s_nop 0
	v_cndmask_b32_e32 v5, v5, v4, vcc
	v_cndmask_b32_e64 v4, 0, 1, vcc
	v_or_b32_e32 v4, v8, v4
	ds_write_b64 v6, v[4:5] offset:48432
